# baseline (speedup 1.0000x reference)
.Lno_anc:
	s_or_b64 exec, exec, s[8:9]
	v_mov_b32_e32 v7, 0x80
	s_waitcnt vmcnt(0)
	s_and_saveexec_b64 s[0:1], vcc
	ds_write_b128 v11, v[2:5] offset:32768
	ds_write_b128 v11, v[44:47] offset:40960
	s_or_b64 exec, exec, s[0:1]
	s_sub_u32 s26, 0xff, s2
	s_mul_i32 s26, s26, 28
	s_lshr_b32 s26, s26, 7
	s_min_u32 s26, s26, 64
	s_cmp_eq_u32 s26, 0
	s_cbranch_scc1 .Lhold_done

.LcompA_end:
	s_or_b64 exec, exec, s[10:11]
	s_ashr_i32 s0, s14, 16
	s_add_i32 s3, s3, s0
	s_mov_b32 s27, s3
	s_waitcnt lgkmcnt(0)
	v_cmp_gt_i32_e32 vcc, s27, v10
	s_and_b64 exec, exec, vcc
	s_mov_b64 s[30:31], exec
	s_cbranch_execz .Lskip_issueA
	v_lshlrev_b32_e32 v3, 1, v10
	v_lshl_or_b32 v3, v1, 10, v3
	v_mov_b32_e32 v4, v10
	ds_read_u16 v5, v3
	s_waitcnt lgkmcnt(0)
	v_add_u32_e32 v8, v6, v5
	v_lshlrev_b32_e32 v8, 4, v8
	global_load_dwordx4 v[48:51], v8, s[16:17] nt
	global_load_dwordx4 v[52:55], v8, s[18:19] nt
	v_lshlrev_b32_e32 v5, 4, v5
.Lskip_issueA:
	s_mov_b64 exec, -1
	v_mov_b32_e32 v12, v26
	v_mov_b32_e32 v13, v27
	v_mov_b32_e32 v14, v28
	v_mov_b32_e32 v15, v29
	v_mov_b32_e32 v16, v30
	v_mov_b32_e32 v17, v31
	v_mov_b32_e32 v18, v32
	v_mov_b32_e32 v19, v33
	v_mov_b32_e32 v7, 0x80
	v_cmp_ne_u32_e64 s[4:5], 0, v12
	s_nop 1
	v_cndmask_b32_e64 v8, 0, 1, s[4:5]
	v_cmp_eq_u32_e64 s[4:5], 0, v13
	s_nop 1
	v_cndmask_b32_e64 v9, 2, 0, s[4:5]
	v_cmp_eq_u32_e64 s[4:5], 0, v14
	v_or_b32_e32 v8, v9, v8
	s_nop 0
	v_cndmask_b32_e64 v12, 4, 0, s[4:5]
	v_cmp_eq_u32_e64 s[4:5], 0, v15
	s_nop 1
	v_cndmask_b32_e64 v13, 8, 0, s[4:5]
	v_cmp_eq_u32_e64 s[4:5], 0, v16
	v_or3_b32 v8, v8, v12, v13
	s_nop 0
	v_cndmask_b32_e64 v14, 16, 0, s[4:5]
	v_cmp_eq_u32_e64 s[4:5], 0, v17
	s_nop 1
	v_cndmask_b32_e64 v15, 32, 0, s[4:5]
	v_cmp_eq_u32_e64 s[4:5], 0, v18
	s_nop 1
	v_cndmask_b32_e64 v16, 64, 0, s[4:5]
	v_cmp_eq_u32_e64 s[4:5], 0, v19
	s_nop 1
	v_cndmask_b32_e64 v7, v7, 0, s[4:5]
	v_or_b32_e32 v7, v16, v7
	v_or3_b32 v9, v7, v15, v14
	v_or_b32_e32 v7, v9, v8
	v_bcnt_u32_b32 v8, v8, 0
	v_bcnt_u32_b32 v9, v9, 0
	v_lshl_or_b32 v9, v9, 16, v8
	v_cmp_ne_u32_e64 s[4:5], 0, v7
	s_nop 0
	v_add_u32_dpp v8, v9, v9 row_shr:1 row_mask:0xf bank_mask:0xf bound_ctrl:1
	s_nop 1
	v_add_u32_dpp v8, v8, v8 row_shr:2 row_mask:0xf bank_mask:0xf bound_ctrl:1
	s_nop 1
	v_add_u32_dpp v8, v8, v8 row_shr:4 row_mask:0xf bank_mask:0xf bound_ctrl:1
	s_nop 1
	v_add_u32_dpp v12, v8, v8 row_shr:8 row_mask:0xf bank_mask:0xf bound_ctrl:1
	s_nop 1
	v_add_u32_dpp v12, v12, v12 row_bcast:15 row_mask:0xa bank_mask:0xf
	s_nop 1
	v_add_u32_dpp v12, v12, v12 row_bcast:31 row_mask:0xc bank_mask:0xf
	s_nop 0
	v_readlane_b32 s14, v12, 63
	s_and_b32 s3, s14, 0xffff
	s_and_saveexec_b64 s[10:11], s[4:5]
	s_cbranch_execz .LcompB_end
	v_sub_u32_e32 v12, v12, v9
	v_lshlrev_b32_e32 v8, 10, v1
	v_add_u32_sdwa v9, sext(v12), s3 dst_sel:DWORD dst_unused:UNUSED_PAD src0_sel:WORD_1 src1_sel:DWORD
	v_and_b32_e32 v12, 0xffff, v12
	v_lshlrev_b32_e32 v13, 2, v10
	s_mov_b64 s[12:13], 0
	v_mov_b32_e32 v14, 0x100

.LcompB_end:
	s_or_b64 exec, exec, s[10:11]
	s_ashr_i32 s0, s14, 16
	s_add_i32 s3, s3, s0
	s_mov_b32 s28, s3
	s_waitcnt lgkmcnt(0)
	v_mov_b32_e32 v2, 0
	v_cmp_gt_i32_e32 vcc, s28, v10
	s_and_b64 exec, exec, vcc
	s_mov_b64 s[32:33], exec
	s_cbranch_execz .Lskip_issueB
	v_lshlrev_b32_e32 v24, 1, v10
	v_lshl_or_b32 v24, v1, 10, v24
	v_mov_b32_e32 v25, v10
	ds_read_u16 v42, v24 offset:16384
	s_waitcnt lgkmcnt(0)
	v_add_u32_e32 v8, v43, v42
	v_lshlrev_b32_e32 v8, 4, v8
	global_load_dwordx4 v[34:37], v8, s[16:17] nt
	global_load_dwordx4 v[38:41], v8, s[18:19] nt
	v_lshlrev_b32_e32 v42, 4, v42
.Lskip_issueB:
	s_mov_b64 exec, -1
	s_barrier
	s_waitcnt vmcnt(0)
	s_mov_b64 exec, s[30:31]
	s_cbranch_execz .Lskip_compA
	v_mov_b32_e32 v12, v48
	v_mov_b32_e32 v13, v49
	v_mov_b32_e32 v14, v50
	v_mov_b32_e32 v15, v51
	v_mov_b32_e32 v16, v52
	v_mov_b32_e32 v17, v53
	v_mov_b32_e32 v18, v54
	v_mov_b32_e32 v19, v55
	ds_read_b128 v[20:23], v5 offset:32768
	s_waitcnt lgkmcnt(0)
	v_pk_add_f32 v[8:9], v[22:23], v[20:21] neg_lo:[0,1] neg_hi:[0,1]
	s_nop 0
	v_pk_fma_f32 v[20:21], v[8:9], 0.5, v[20:21] op_sel_hi:[1,0,1]
	s_waitcnt vmcnt(1)
	v_mul_f32_e32 v5, 0x3fb8aa3b, v14
	v_mul_f32_e32 v7, 0x3fb8aa3b, v15
	v_pk_fma_f32 v[12:13], v[12:13], v[8:9], v[20:21]
	s_waitcnt vmcnt(0)
	v_sub_f32_e32 v14, v18, v16
	v_sub_f32_e32 v20, v19, v17
	v_max_f32_e32 v11, v18, v18
	v_max_f32_e32 v15, v16, v16
	v_max_f32_e32 v18, v19, v19
	v_max_f32_e32 v19, v17, v17
	v_exp_f32_e32 v16, v5
	v_exp_f32_e32 v17, v7
	s_nop 0
	v_pk_mul_f32 v[8:9], v[16:17], v[8:9]
	s_nop 0
	v_pk_fma_f32 v[16:17], v[8:9], 0.5, v[12:13] op_sel_hi:[1,0,1] neg_lo:[1,0,0] neg_hi:[1,0,0]
	v_pk_fma_f32 v[8:9], v[8:9], 0.5, v[12:13] op_sel_hi:[1,0,1]
	v_max_f32_e32 v7, v16, v15
	v_min_f32_e32 v5, v8, v11
	v_min_f32_e32 v21, v9, v18
	v_max_f32_e32 v22, v17, v19
	v_pk_add_f32 v[12:13], v[8:9], v[16:17] neg_lo:[0,1] neg_hi:[0,1]
	v_max_f32_e32 v8, v8, v11
	v_min_f32_e32 v11, v16, v15
	v_max_f32_e32 v9, v9, v18
	v_min_f32_e32 v15, v17, v19
	v_sub_f32_e32 v5, v5, v7
	v_sub_f32_e32 v7, v21, v22
	v_sub_f32_e32 v8, v8, v11
	v_sub_f32_e32 v9, v9, v15
	v_max_f32_e32 v15, 0, v5
	v_max_f32_e32 v21, 0, v7
	v_max_f32_e32 v5, 0, v8
	v_max_f32_e32 v7, 0, v9
	v_pk_mul_f32 v[8:9], v[14:15], v[20:21]
	v_mul_f32_e32 v11, v5, v7
	v_fma_f32 v8, v12, v13, v8
	v_sub_f32_e32 v8, v8, v9
	v_rcp_f32_e32 v14, v11
	v_rcp_f32_e32 v15, v8
	v_fma_f32 v8, v5, v7, -v8
	v_pk_mul_f32 v[8:9], v[14:15], v[8:9]
	s_nop 0
	v_sub_f32_e32 v5, v8, v9
	v_add_f32_e32 v5, 1.0, v5
	v_add_f32_e32 v2, v2, v5

	.amdhsa_kernel _Z12giou_partialPK15HIP_vector_typeIfLj4EES2_S2_PKiPS_IfLj2EE
		.amdhsa_group_segment_fixed_size 49280
		.amdhsa_private_segment_fixed_size 0
		.amdhsa_kernarg_size 40
		.amdhsa_user_sgpr_count 2
		.amdhsa_user_sgpr_dispatch_ptr 0
		.amdhsa_user_sgpr_queue_ptr 0
		.amdhsa_user_sgpr_kernarg_segment_ptr 1
		.amdhsa_user_sgpr_dispatch_id 0
		.amdhsa_user_sgpr_kernarg_preload_length 0
		.amdhsa_user_sgpr_kernarg_preload_offset 0
		.amdhsa_user_sgpr_private_segment_size 0
		.amdhsa_uses_dynamic_stack 0
		.amdhsa_enable_private_segment 0
		.amdhsa_system_sgpr_workgroup_id_x 1
		.amdhsa_system_sgpr_workgroup_id_y 0
		.amdhsa_system_sgpr_workgroup_id_z 0
		.amdhsa_system_sgpr_workgroup_info 0
		.amdhsa_system_vgpr_workitem_id 0
		.amdhsa_next_free_vgpr 56
		.amdhsa_next_free_sgpr 34
		.amdhsa_accum_offset 56
		.amdhsa_reserve_vcc 1
		.amdhsa_float_round_mode_32 0
		.amdhsa_float_round_mode_16_64 0
		.amdhsa_float_denorm_mode_32 3
		.amdhsa_float_denorm_mode_16_64 3
		.amdhsa_dx10_clamp 1
		.amdhsa_ieee_mode 1
		.amdhsa_fp16_overflow 0
		.amdhsa_tg_split 0
		.amdhsa_exception_fp_ieee_invalid_op 0
		.amdhsa_exception_fp_denorm_src 0
		.amdhsa_exception_fp_ieee_div_zero 0
		.amdhsa_exception_fp_ieee_overflow 0
		.amdhsa_exception_fp_ieee_underflow 0
		.amdhsa_exception_fp_ieee_inexact 0
		.amdhsa_exception_int_div_zero 0
	.end_amdhsa_kernel

.Lfunc_end0:
	.size	_Z12giou_partialPK15HIP_vector_typeIfLj4EES2_S2_PKiPS_IfLj2EE, .Lfunc_end0-_Z12giou_partialPK15HIP_vector_typeIfLj4EES2_S2_PKiPS_IfLj2EE
	.set _Z12giou_partialPK15HIP_vector_typeIfLj4EES2_S2_PKiPS_IfLj2EE.num_vgpr, 56
	.set _Z12giou_partialPK15HIP_vector_typeIfLj4EES2_S2_PKiPS_IfLj2EE.num_agpr, 0
	.set _Z12giou_partialPK15HIP_vector_typeIfLj4EES2_S2_PKiPS_IfLj2EE.numbered_sgpr, 34
	.set _Z12giou_partialPK15HIP_vector_typeIfLj4EES2_S2_PKiPS_IfLj2EE.num_named_barrier, 0
	.set _Z12giou_partialPK15HIP_vector_typeIfLj4EES2_S2_PKiPS_IfLj2EE.private_seg_size, 0
	.set _Z12giou_partialPK15HIP_vector_typeIfLj4EES2_S2_PKiPS_IfLj2EE.uses_vcc, 1
	.set _Z12giou_partialPK15HIP_vector_typeIfLj4EES2_S2_PKiPS_IfLj2EE.uses_flat_scratch, 0
	.set _Z12giou_partialPK15HIP_vector_typeIfLj4EES2_S2_PKiPS_IfLj2EE.has_dyn_sized_stack, 0
	.set _Z12giou_partialPK15HIP_vector_typeIfLj4EES2_S2_PKiPS_IfLj2EE.has_recursion, 0
	.set _Z12giou_partialPK15HIP_vector_typeIfLj4EES2_S2_PKiPS_IfLj2EE.has_indirect_call, 0

amdhsa.kernels:
  - .agpr_count:     0
    .args:
      - .actual_access:  read_only
        .address_space:  global
        .offset:         0
        .size:           8
        .value_kind:     global_buffer
      - .actual_access:  read_only
        .address_space:  global
        .offset:         8
        .size:           8
        .value_kind:     global_buffer
      - .actual_access:  read_only
        .address_space:  global
        .offset:         16
        .size:           8
        .value_kind:     global_buffer
      - .actual_access:  read_only
        .address_space:  global
        .offset:         24
        .size:           8
        .value_kind:     global_buffer
      - .actual_access:  write_only
        .address_space:  global
        .offset:         32
        .size:           8
        .value_kind:     global_buffer
    .group_segment_fixed_size: 49280
    .kernarg_segment_align: 8
    .kernarg_segment_size: 40
    .language:       OpenCL C
    .language_version:
      - 2
      - 0
    .max_flat_workgroup_size: 1024
    .name:           _Z12giou_partialPK15HIP_vector_typeIfLj4EES2_S2_PKiPS_IfLj2EE
    .private_segment_fixed_size: 0
    .sgpr_count:     40
    .sgpr_spill_count: 0
    .symbol:         _Z12giou_partialPK15HIP_vector_typeIfLj4EES2_S2_PKiPS_IfLj2EE.kd
    .uniform_work_group_size: 1
    .uses_dynamic_stack: false
    .vgpr_count:     56
    .vgpr_spill_count: 0
    .wavefront_size: 64
  - .agpr_count:     0
    .args:
      - .actual_access:  read_only
        .address_space:  global
        .offset:         0
        .size:           8
        .value_kind:     global_buffer
      - .actual_access:  write_only
        .address_space:  global
        .offset:         8
        .size:           8
        .value_kind:     global_buffer
    .group_segment_fixed_size: 0
    .kernarg_segment_align: 8
    .kernarg_segment_size: 16
    .language:       OpenCL C
    .language_version:
      - 2
      - 0
    .max_flat_workgroup_size: 64
    .name:           _Z10giou_finalPK15HIP_vector_typeIfLj2EEPf
    .private_segment_fixed_size: 0
    .sgpr_count:     18
    .sgpr_spill_count: 0
    .symbol:         _Z10giou_finalPK15HIP_vector_typeIfLj2EEPf.kd
    .uniform_work_group_size: 1
    .uses_dynamic_stack: false
    .vgpr_count:     18
    .vgpr_spill_count: 0
    .wavefront_size: 64
